# attention phase: static s_setprio 1 for waves 0-3 (the other half)
# speedup vs baseline: 1.0090x; 1.0090x over previous
; #define LAS __attribute__((address_space(3)))
;     DI unsigned char* wsp() const { return (unsigned char*)ws_g; }
;     DI const float* inp(int i) const { return (const float*)(*(const GAS float* const __attribute__((address_space(4)))*)(ka + 8 * i)); }
;     static constexpr unsigned PIECES[NPIECE] = {1179905,1638914,786432,2032387,2032644,2032901,2033158,2033415,2033672,2033929,2034186,2034443,2034700,2034957,2035214,2035471,2035728,2034944,2035985,2036242,2036499,2036756,2037013,2037270,2037527,2037784,2038041,2036481,2038298,2038555,2038812,2039069,2039326,2039583,2038274};
;     LAS unsigned char* Ks = F.lds;
;     LAS unsigned char* Vt = F.lds + 36864;
;     LAS float* LUT = (LAS float*)(F.lds + 36864 + 33280);
;     LAS unsigned* CTL = (LAS unsigned*)(F.lds + 36864 + 33280 + 528);
;     LAS unsigned* LIST = CTL + 4;
;     const bf16_t* MO = (const bf16_t*)(F.wsp() + WS_MO); const unsigned* SEL = (const unsigned*)(F.wsp() + WS_SEL);
;     bf16_t* PO = (bf16_t*)(F.wsp() + WS_PO); f32x2* PST = (f32x2*)(F.wsp() + WS_PST);
;     unsigned* qctr = (unsigned*)(F.wsp() + WS_CTL) + CW_QATT + 64 * l + 32 * rep;
;     const float* relb = F.inp(25);
;     const int lane = F.lane;
;     bool att_done = false, conv_done = false;
;     unsigned nu = 0u; if (F.tid == 0) nu = __hip_atomic_fetch_add(qctr, 1u, __ATOMIC_RELAXED, __HIP_MEMORY_SCOPE_AGENT);
.LBB0_1782:
	s_cmp_le_i32 s96, s22
	s_cselect_b64 s[2:3], -1, 0
	s_and_b64 s[36:37], s[2:3], s[0:1]
	v_readlane_b32 s0, v252, 17
	v_readlane_b32 s1, v252, 18
	v_readlane_b32 s2, v252, 19
	v_readlane_b32 s3, v252, 20
	s_andn2_b64 vcc, exec, s[36:37]
	v_writelane_b32 v252, s2, 19
	s_nop 1
	v_writelane_b32 v252, s3, 20
	v_writelane_b32 v252, s0, 17
	s_nop 1
	v_writelane_b32 v252, s1, 18
	s_cbranch_vccnz .LBB0_2249
	s_lshl_b32 s44, s50, 6
	s_lshl_b64 s[0:1], s[44:45], 2
	s_add_u32 s0, s94, s0
	s_addc_u32 s1, s95, s1
	v_mov_b32_e32 v0, v230
	s_add_u32 s38, s0, 0x8000
	s_addc_u32 s39, s1, 0
	v_lshl_add_u32 v147, s68, 6, v0
	s_cmp_lt_u32 s68, 4
	s_cbranch_scc0 .Lattn_prio_done
	s_setprio 1
